# phase D elementwise loop: touch loads for the next trip's rows behind each trip's own loads
# baseline (speedup 1.0000x reference)
.LBB0_640:
	v_ashrrev_i32_e32 v0, 7, v79
	v_add_u32_e32 v58, s28, v0
	v_ashrrev_i32_e32 v59, 31, v58
	v_lshlrev_b64 v[6:7], 11, v[58:59]
	s_and_saveexec_b64 s[40:41], s[6:7]
	s_xor_b64 s[72:73], exec, s[40:41]
	s_cbranch_execz .LBB0_642
	v_lshl_add_u64 v[2:3], v[40:41], 0, v[6:7]
	v_lshl_add_u64 v[4:5], v[42:43], 0, v[6:7]
	s_mov_b32 s100, 0x2000
	s_mov_b32 s101, 0
	v_lshl_add_u64 v[160:161], v[2:3], 0, s[100:101]
	v_lshl_add_u64 v[162:163], v[4:5], 0, s[100:101]
	global_load_dwordx4 v[64:67], v[2:3], off
	global_load_dwordx4 v[68:71], v[4:5], off
	v_add_co_u32_e32 v2, vcc, 0x1100000, v2
	s_mov_b32 s36, 0x88000
	s_nop 0
	v_addc_co_u32_e32 v3, vcc, 0, v3, vcc
	global_load_dwordx4 v[80:83], v[2:3], off
	v_lshlrev_b64 v[2:3], 6, v[58:59]
	v_lshl_add_u64 v[4:5], s[34:35], 0, v[2:3]
	v_lshl_add_u64 v[4:5], v[4:5], 0, v[104:105]
	v_add_co_u32_e32 v6, vcc, s36, v4
	v_mad_u64_u32 v[0:1], s[40:41], v0, s53, v[36:37]
	s_nop 0
	v_addc_co_u32_e32 v7, vcc, 0, v5, vcc
	ds_read_b128 v[0:3], v0 offset:8704
	global_load_dword v21, v[4:5], off
	global_load_dword v94, v[6:7], off
	global_load_dwordx4 v[8:11], v[44:45], off offset:16
	global_load_dwordx4 v[12:15], v[44:45], off
	s_nop 0
	global_load_dwordx4 v[4:7], v[46:47], off offset:16
	global_load_dwordx4 v[16:19], v[46:47], off
	s_mov_b32 s100, 0x1100000
	global_load_dword v166, v[160:161], off
	global_load_dword v166, v[162:163], off
	v_lshl_add_u64 v[164:165], v[160:161], 0, s[100:101]
	global_load_dword v166, v[164:165], off
	s_mov_b32 s36, 0x3c800000
	s_waitcnt lgkmcnt(0)
	v_lshlrev_b32_e32 v22, 16, v2
	v_and_b32_e32 v23, 0xffff0000, v2
	v_lshlrev_b32_e32 v26, 16, v0
	v_and_b32_e32 v27, 0xffff0000, v0
	v_lshlrev_b32_e32 v0, 16, v1
	v_and_b32_e32 v1, 0xffff0000, v1
	s_waitcnt vmcnt(11)
	v_lshlrev_b32_e32 v63, 16, v67
	v_and_b32_e32 v84, 0xffff0000, v67
	v_lshlrev_b32_e32 v86, 16, v64
	v_and_b32_e32 v87, 0xffff0000, v64
	v_lshlrev_b32_e32 v90, 16, v66
	v_and_b32_e32 v91, 0xffff0000, v66
	s_waitcnt vmcnt(10)
	v_lshlrev_b32_e32 v95, 16, v71
	s_waitcnt vmcnt(9)
	v_and_b32_e32 v85, 0xffff0000, v83
	v_lshlrev_b32_e32 v66, 16, v80
	v_and_b32_e32 v67, 0xffff0000, v80
	v_and_b32_e32 v20, 0xffff0000, v71
	v_lshlrev_b32_e32 v60, 16, v68
	v_and_b32_e32 v61, 0xffff0000, v68
	v_lshlrev_b32_e32 v88, 16, v65
	v_and_b32_e32 v89, 0xffff0000, v65
	v_lshlrev_b32_e32 v64, 16, v69
	v_and_b32_e32 v65, 0xffff0000, v69
	v_lshlrev_b32_e32 v24, 16, v70
	v_and_b32_e32 v25, 0xffff0000, v70
	v_lshlrev_b32_e32 v2, 16, v83
	v_lshlrev_b32_e32 v68, 16, v81
	v_and_b32_e32 v69, 0xffff0000, v81
	v_lshlrev_b32_e32 v80, 16, v82
	v_and_b32_e32 v81, 0xffff0000, v82
	v_pk_mov_b32 v[82:83], v[84:85], v[84:85] op_sel:[1,0]
	v_pk_add_f32 v[70:71], v[86:87], v[66:67]
	v_pk_add_f32 v[66:67], v[90:91], v[80:81]
	v_mov_b32_e32 v83, v2
	v_add_f32_e32 v81, 0, v70
	v_mul_f32_e32 v2, v71, v71
	v_pk_add_f32 v[68:69], v[88:89], v[68:69]
	v_add_f32_e32 v81, v71, v81
	v_pk_fma_f32 v[88:89], v[70:71], v[70:71], v[2:3] op_sel_hi:[1,1,0]
	v_mul_f32_e32 v80, v69, v69
	v_add_f32_e32 v2, v68, v81
	v_pk_fma_f32 v[88:89], v[68:69], v[68:69], v[88:89]
	v_mov_b32_e32 v62, v84
	v_add_f32_e32 v2, v69, v2
	v_pk_add_f32 v[80:81], v[80:81], v[88:89] op_sel_hi:[0,1]
	v_mov_b32_e32 v92, v84
	v_mov_b32_e32 v93, v67
	v_mul_f32_e32 v86, v67, v67
	v_pk_add_f32 v[62:63], v[82:83], v[62:63]
	v_add_f32_e32 v83, v66, v2
	v_pk_fma_f32 v[80:81], v[66:67], v[66:67], v[80:81]
	v_pk_mul_f32 v[90:91], v[62:63], v[62:63]
	v_pk_add_f32 v[80:81], v[86:87], v[80:81] op_sel_hi:[0,1]
	v_pk_add_f32 v[82:83], v[92:93], v[82:83]
	v_pk_mov_b32 v[90:91], v[90:91], v[84:85] op_sel:[1,0]
	v_mov_b32_e32 v81, v85
	v_pk_mul_f32 v[84:85], v[62:63], v[82:83]
	v_pk_add_f32 v[82:83], v[62:63], v[82:83]
	v_pk_add_f32 v[80:81], v[90:91], v[80:81]
	v_mov_b32_e32 v85, v83
	v_pk_add_f32 v[80:81], v[84:85], v[80:81]
	s_nop 1
	v_mov_b32_dpp v83, v81 quad_perm:[1,0,3,2] row_mask:0xf bank_mask:0xf bound_ctrl:1
	v_mov_b32_dpp v82, v80 quad_perm:[1,0,3,2] row_mask:0xf bank_mask:0xf bound_ctrl:1
	v_pk_add_f32 v[80:81], v[80:81], v[82:83]
	s_nop 1
	v_mov_b32_dpp v83, v81 quad_perm:[2,3,0,1] row_mask:0xf bank_mask:0xf bound_ctrl:1
	v_mov_b32_dpp v82, v80 quad_perm:[2,3,0,1] row_mask:0xf bank_mask:0xf bound_ctrl:1
	v_pk_add_f32 v[80:81], v[80:81], v[82:83]
	s_nop 1
	v_mov_b32_dpp v83, v81 row_half_mirror row_mask:0xf bank_mask:0xf bound_ctrl:1
	v_mov_b32_dpp v82, v80 row_half_mirror row_mask:0xf bank_mask:0xf bound_ctrl:1
	v_pk_add_f32 v[80:81], v[80:81], v[82:83]
	s_waitcnt vmcnt(7)
	v_add_f32_e32 v82, v21, v94
	v_pk_mul_f32 v[80:81], v[80:81], s[36:37] op_sel_hi:[1,0]
	s_waitcnt vmcnt(6)
	v_mov_b32_e32 v21, v11
	v_fma_f32 v2, -v81, v81, v80
	v_max_f32_e32 v2, 0, v2
	v_add_f32_e32 v2, 0x3a27c5ac, v2
	v_rsq_f32_e32 v2, v2
	v_pk_add_f32 v[70:71], v[70:71], v[80:81] op_sel:[0,1] neg_lo:[0,1] neg_hi:[0,1]
	v_pk_add_f32 v[68:69], v[68:69], v[80:81] op_sel:[0,1] neg_lo:[0,1] neg_hi:[0,1]
	v_pk_mul_f32 v[70:71], v[70:71], v[2:3] op_sel_hi:[1,0]
	s_waitcnt vmcnt(3)
	v_pk_fma_f32 v[12:13], v[12:13], v[70:71], v[16:17]
	v_pk_mul_f32 v[68:69], v[68:69], v[2:3] op_sel_hi:[1,0]
	v_pk_fma_f32 v[12:13], v[82:83], v[60:61], v[12:13] op_sel_hi:[0,1,1]
	v_pk_mul_f32 v[60:61], v[12:13], v[26:27]
	v_pk_add_f32 v[12:13], v[66:67], v[80:81] op_sel:[0,1] neg_lo:[0,1] neg_hi:[0,1]
	v_pk_fma_f32 v[14:15], v[14:15], v[68:69], v[18:19]
	v_pk_mul_f32 v[12:13], v[12:13], v[2:3] op_sel_hi:[1,0]
	v_pk_fma_f32 v[14:15], v[82:83], v[64:65], v[14:15] op_sel_hi:[0,1,1]
	v_pk_fma_f32 v[4:5], v[8:9], v[12:13], v[4:5]
	v_sub_f32_e32 v9, v62, v81
	v_pk_fma_f32 v[4:5], v[82:83], v[24:25], v[4:5] op_sel_hi:[0,1,1]
	v_sub_f32_e32 v8, v63, v81
	v_mul_f32_e32 v83, v9, v2
	v_mul_f32_e32 v8, v8, v2
	v_pk_mul_f32 v[12:13], v[82:83], v[20:21]
	v_mul_f32_e32 v8, v10, v8
	v_mov_b32_e32 v9, v13
	v_mul_f32_e32 v10, v82, v95
	v_pk_add_f32 v[6:7], v[6:7], v[8:9]
	v_mov_b32_e32 v11, v12
	v_lshlrev_b32_e32 v2, 16, v3
	v_and_b32_e32 v3, 0xffff0000, v3
	v_pk_add_f32 v[6:7], v[10:11], v[6:7]
	v_pk_mul_f32 v[0:1], v[14:15], v[0:1]
	v_pk_mul_f32 v[4:5], v[4:5], v[22:23]
	v_pk_mul_f32 v[2:3], v[6:7], v[2:3]
.LBB0_642:
	s_andn2_saveexec_b64 s[72:73], s[72:73]
	s_cbranch_execz .LBB0_639
	v_mad_i64_i32 v[0:1], s[40:41], v58, s95, v[56:57]
	s_mov_b32 s100, 0xb000
	s_mov_b32 s101, 0
	v_lshl_add_u64 v[160:161], v[0:1], 0, s[100:101]
	s_mov_b32 s100, 0x2000
	global_load_dwordx4 v[0:3], v[0:1], off offset:2048
	v_lshl_add_u64 v[12:13], v[48:49], 0, v[6:7]
	v_lshl_add_u64 v[16:17], v[50:51], 0, v[6:7]
	v_lshl_add_u64 v[162:163], v[12:13], 0, s[100:101]
	v_lshl_add_u64 v[164:165], v[16:17], 0, s[100:101]
	global_load_dwordx4 v[4:7], v[12:13], off
	global_load_dwordx4 v[8:11], v[16:17], off
	v_add_co_u32_e32 v12, vcc, s42, v12
	s_waitcnt vmcnt(2)
	v_lshlrev_b32_e32 v68, 16, v0
	v_addc_co_u32_e32 v13, vcc, 0, v13, vcc
	global_load_dwordx4 v[12:15], v[12:13], off
	v_add_co_u32_e32 v16, vcc, s42, v16
	v_and_b32_e32 v69, 0xffff0000, v0
	s_nop 0
	v_addc_co_u32_e32 v17, vcc, 0, v17, vcc
	global_load_dwordx4 v[16:19], v[16:17], off
	s_nop 0
	global_load_dwordx4 v[20:23], v[52:53], off offset:16
	global_load_dwordx4 v[60:63], v[52:53], off
	global_load_dwordx4 v[24:27], v[54:55], off offset:16
	global_load_dwordx4 v[64:67], v[54:55], off
	s_mov_b32 s100, s42
	global_load_dword v166, v[160:161], off offset:2048
	global_load_dword v166, v[162:163], off
	global_load_dword v166, v[164:165], off
	v_lshl_add_u64 v[162:163], v[162:163], 0, s[100:101]
	v_lshl_add_u64 v[164:165], v[164:165], 0, s[100:101]
	global_load_dword v166, v[162:163], off
	global_load_dword v166, v[164:165], off
	v_mul_f32_e32 v0, 0x3d372713, v68
	s_waitcnt vmcnt(12)
	v_lshlrev_b32_e32 v70, 16, v4
	v_and_b32_e32 v71, 0xffff0000, v4
	v_mul_f32_e32 v0, v0, v68
	v_mov_b32_e32 v4, v68
	v_fmac_f32_e32 v4, v0, v4
	v_mul_f32_e32 v0, 0x3f4c422a, v4
	v_add_f32_e32 v0, v0, v0
	v_mul_f32_e32 v0, 0x3fb8aa3b, v0
	v_exp_f32_e32 v0, v0
	s_waitcnt vmcnt(11)
	v_lshlrev_b32_e32 v80, 16, v8
	v_and_b32_e32 v81, 0xffff0000, v8
	v_lshlrev_b32_e32 v4, 16, v5
	v_add_f32_e32 v0, 1.0, v0
	v_and_b32_e32 v5, 0xffff0000, v5
	v_lshlrev_b32_e32 v8, 16, v9
	v_and_b32_e32 v9, 0xffff0000, v9
	s_waitcnt vmcnt(10)
	v_lshlrev_b32_e32 v82, 16, v12
	v_and_b32_e32 v83, 0xffff0000, v12
	s_waitcnt vmcnt(9)
	v_lshlrev_b32_e32 v84, 16, v16
	v_and_b32_e32 v85, 0xffff0000, v16
	s_waitcnt vmcnt(7)
	v_pk_fma_f32 v[60:61], v[60:61], v[80:81], v[70:71]
	v_pk_mul_f32 v[70:71], v[68:69], 0.5 op_sel_hi:[1,0]
	v_pk_add_f32 v[60:61], v[60:61], v[82:83]
	v_lshlrev_b32_e32 v12, 16, v13
	s_waitcnt vmcnt(5)
	v_pk_fma_f32 v[60:61], v[64:65], v[84:85], v[60:61]
	v_rcp_f32_e32 v64, v0
	v_mul_f32_e32 v0, 0x3d372713, v69
	v_mul_f32_e32 v0, v0, v69
	v_fmac_f32_e32 v69, v0, v69
	v_mul_f32_e32 v0, 0x3f4c422a, v69
	v_add_f32_e32 v0, v0, v0
	v_mul_f32_e32 v0, 0x3fb8aa3b, v0
	v_exp_f32_e32 v0, v0
	v_and_b32_e32 v13, 0xffff0000, v13
	v_pk_fma_f32 v[4:5], v[62:63], v[8:9], v[4:5]
	v_lshlrev_b32_e32 v16, 16, v17
	v_add_f32_e32 v0, 1.0, v0
	v_rcp_f32_e32 v65, v0
	v_lshlrev_b32_e32 v0, 16, v1
	v_and_b32_e32 v1, 0xffff0000, v1
	v_mul_f32_e32 v8, 0x3d372713, v0
	v_pk_add_f32 v[4:5], v[4:5], v[12:13]
	v_mul_f32_e32 v8, v8, v0
	v_mov_b32_e32 v9, v0
	v_pk_mul_f32 v[12:13], v[0:1], 0.5 op_sel_hi:[1,0]
	v_mul_f32_e32 v0, 0x3d372713, v1
	v_mul_f32_e32 v0, v0, v1
	v_fmac_f32_e32 v9, v8, v9
	v_fmac_f32_e32 v1, v0, v1
	v_mul_f32_e32 v8, 0x3f4c422a, v9
	v_mul_f32_e32 v0, 0x3f4c422a, v1
	v_add_f32_e32 v8, v8, v8
	v_add_f32_e32 v0, v0, v0
	v_mul_f32_e32 v8, 0x3fb8aa3b, v8
	v_mul_f32_e32 v0, 0x3fb8aa3b, v0
	v_exp_f32_e32 v8, v8
	v_exp_f32_e32 v0, v0
	v_and_b32_e32 v17, 0xffff0000, v17
	v_pk_fma_f32 v[4:5], v[66:67], v[16:17], v[4:5]
	v_add_f32_e32 v8, 1.0, v8
	v_add_f32_e32 v0, 1.0, v0
	v_rcp_f32_e32 v8, v8
	v_rcp_f32_e32 v9, v0
	v_lshlrev_b32_e32 v16, 16, v14
	v_and_b32_e32 v17, 0xffff0000, v14
	v_lshlrev_b32_e32 v62, 16, v18
	v_pk_fma_f32 v[0:1], v[8:9], 2.0, 1.0 op_sel_hi:[1,0,0] neg_lo:[1,0,0] neg_hi:[1,0,0]
	v_lshlrev_b32_e32 v8, 16, v6
	v_pk_add_f32 v[0:1], v[0:1], 1.0 op_sel_hi:[1,0]
	v_and_b32_e32 v9, 0xffff0000, v6
	v_pk_mul_f32 v[0:1], v[12:13], v[0:1]
	v_lshlrev_b32_e32 v12, 16, v10
	v_pk_mul_f32 v[0:1], v[4:5], v[0:1]
	v_lshlrev_b32_e32 v4, 16, v2
	v_and_b32_e32 v5, 0xffff0000, v2
	v_mul_f32_e32 v2, 0x3d372713, v4
	v_mul_f32_e32 v2, v2, v4
	v_mov_b32_e32 v6, v4
	v_fmac_f32_e32 v6, v2, v6
	v_mul_f32_e32 v2, 0x3f4c422a, v6
	v_add_f32_e32 v2, v2, v2
	v_mul_f32_e32 v2, 0x3fb8aa3b, v2
	v_exp_f32_e32 v2, v2
	v_and_b32_e32 v13, 0xffff0000, v10
	v_pk_fma_f32 v[8:9], v[20:21], v[12:13], v[8:9]
	v_and_b32_e32 v63, 0xffff0000, v18
	v_add_f32_e32 v2, 1.0, v2
	v_rcp_f32_e32 v12, v2
	v_mul_f32_e32 v2, 0x3d372713, v5
	v_mul_f32_e32 v2, v2, v5
	v_pk_add_f32 v[8:9], v[8:9], v[16:17]
	v_pk_mul_f32 v[16:17], v[4:5], 0.5 op_sel_hi:[1,0]
	v_fmac_f32_e32 v5, v2, v5
	v_mul_f32_e32 v2, 0x3f4c422a, v5
	v_add_f32_e32 v2, v2, v2
	v_mul_f32_e32 v2, 0x3fb8aa3b, v2
	v_exp_f32_e32 v2, v2
	v_pk_fma_f32 v[8:9], v[24:25], v[62:63], v[8:9]
	v_lshlrev_b32_e32 v6, 16, v7
	v_and_b32_e32 v7, 0xffff0000, v7
	v_add_f32_e32 v2, 1.0, v2
	v_rcp_f32_e32 v13, v2
	v_lshlrev_b32_e32 v2, 16, v3
	v_and_b32_e32 v3, 0xffff0000, v3
	v_lshlrev_b32_e32 v10, 16, v15
	v_pk_fma_f32 v[4:5], v[12:13], 2.0, 1.0 op_sel_hi:[1,0,0] neg_lo:[1,0,0] neg_hi:[1,0,0]
	v_pk_fma_f32 v[64:65], v[64:65], 2.0, 1.0 op_sel_hi:[1,0,0] neg_lo:[1,0,0] neg_hi:[1,0,0]
	v_pk_add_f32 v[4:5], v[4:5], 1.0 op_sel_hi:[1,0]
	v_pk_add_f32 v[64:65], v[64:65], 1.0 op_sel_hi:[1,0]
	v_pk_mul_f32 v[4:5], v[16:17], v[4:5]
	v_lshlrev_b32_e32 v12, 16, v19
	v_pk_mul_f32 v[4:5], v[8:9], v[4:5]
	v_lshlrev_b32_e32 v8, 16, v11
	v_and_b32_e32 v9, 0xffff0000, v11
	v_and_b32_e32 v11, 0xffff0000, v15
	v_pk_fma_f32 v[6:7], v[22:23], v[8:9], v[6:7]
	v_mul_f32_e32 v8, 0x3d372713, v2
	v_pk_add_f32 v[6:7], v[6:7], v[10:11]
	v_mul_f32_e32 v8, v8, v2
	v_mov_b32_e32 v9, v2
	v_pk_mul_f32 v[10:11], v[2:3], 0.5 op_sel_hi:[1,0]
	v_mul_f32_e32 v2, 0x3d372713, v3
	v_mul_f32_e32 v2, v2, v3
	v_fmac_f32_e32 v9, v8, v9
	v_fmac_f32_e32 v3, v2, v3
	v_mul_f32_e32 v8, 0x3f4c422a, v9
	v_mul_f32_e32 v2, 0x3f4c422a, v3
	v_add_f32_e32 v8, v8, v8
	v_add_f32_e32 v2, v2, v2
	v_mul_f32_e32 v8, 0x3fb8aa3b, v8
	v_mul_f32_e32 v2, 0x3fb8aa3b, v2
	v_exp_f32_e32 v8, v8
	v_exp_f32_e32 v2, v2
	v_and_b32_e32 v13, 0xffff0000, v19
	v_pk_mul_f32 v[64:65], v[70:71], v[64:65]
	v_add_f32_e32 v8, 1.0, v8
	v_add_f32_e32 v2, 1.0, v2
	v_rcp_f32_e32 v8, v8
	v_rcp_f32_e32 v9, v2
	v_pk_fma_f32 v[6:7], v[26:27], v[12:13], v[6:7]
	v_pk_mul_f32 v[60:61], v[60:61], v[64:65]
	v_pk_fma_f32 v[2:3], v[8:9], 2.0, 1.0 op_sel_hi:[1,0,0] neg_lo:[1,0,0] neg_hi:[1,0,0]
	s_nop 0
	v_pk_add_f32 v[2:3], v[2:3], 1.0 op_sel_hi:[1,0]
	s_nop 0
	v_pk_mul_f32 v[2:3], v[10:11], v[2:3]
	s_nop 0
	v_pk_mul_f32 v[2:3], v[6:7], v[2:3]
	s_branch .LBB0_639
